# baseline (speedup 1.0000x reference)
.Lmpart_c:
	s_cmp_eq_u32 s35, 7
	s_cbranch_scc1 .Lmd1_c
	v_sub_u32_e32 v84, v219, v228
	v_cmp_lt_i32_e32 vcc, 0xc0, v84
	s_nop 1
	v_cndmask_b32_e32 v67, v241, v99, vcc
	v_cmp_le_i32_e32 vcc, 0xc0, v84
	s_nop 1
	v_cndmask_b32_e32 v66, v241, v98, vcc
	v_cmp_le_i32_e32 vcc, 0xc2, v84
	s_nop 1
	v_cndmask_b32_e32 v68, v241, v100, vcc
	v_cmp_le_i32_e32 vcc, 0xc3, v84
	s_nop 1
	v_cndmask_b32_e32 v69, v241, v101, vcc
	v_cmp_le_i32_e32 vcc, 0xc8, v84
	s_nop 1
	v_cndmask_b32_e32 v70, v241, v102, vcc
	v_cmp_le_i32_e32 vcc, 0xc9, v84
	s_nop 1
	v_cndmask_b32_e32 v71, v241, v103, vcc
	v_cmp_le_i32_e32 vcc, 0xca, v84
	s_nop 1
	v_cndmask_b32_e32 v72, v241, v104, vcc
	v_cmp_le_i32_e32 vcc, 0xcb, v84
	s_nop 1
	v_cndmask_b32_e32 v73, v241, v105, vcc
	v_cmp_le_i32_e32 vcc, 0xd0, v84
	s_nop 1
	v_cndmask_b32_e32 v74, v241, v106, vcc
	v_cmp_le_i32_e32 vcc, 0xd1, v84
	s_nop 1
	v_cndmask_b32_e32 v75, v241, v107, vcc
	v_cmp_le_i32_e32 vcc, 0xd2, v84
	s_nop 1
	v_cndmask_b32_e32 v76, v241, v108, vcc
	v_cmp_le_i32_e32 vcc, 0xd3, v84
	s_nop 1
	v_cndmask_b32_e32 v77, v241, v109, vcc
	v_cmp_le_i32_e32 vcc, 0xd8, v84
	s_nop 1
	v_cndmask_b32_e32 v78, v241, v110, vcc
	v_cmp_le_i32_e32 vcc, 0xd9, v84
	s_nop 1
	v_cndmask_b32_e32 v79, v241, v111, vcc
	v_cmp_le_i32_e32 vcc, 0xda, v84
	s_nop 1
	v_cndmask_b32_e32 v80, v241, v112, vcc
	v_cmp_le_i32_e32 vcc, 0xdb, v84
	s_nop 1
	v_cndmask_b32_e32 v81, v241, v113, vcc
	v_mov_b32_e32 v50, v241
	v_mov_b32_e32 v51, v241
	v_mov_b32_e32 v52, v241
	v_mov_b32_e32 v53, v241
	v_mov_b32_e32 v54, v241
	v_mov_b32_e32 v55, v241
	v_mov_b32_e32 v56, v241
	v_mov_b32_e32 v57, v241
	v_mov_b32_e32 v58, v241
	v_mov_b32_e32 v59, v241
	v_mov_b32_e32 v60, v241
	v_mov_b32_e32 v61, v241
	v_mov_b32_e32 v62, v241
	v_mov_b32_e32 v63, v241
	v_mov_b32_e32 v64, v241
	v_mov_b32_e32 v65, v241
	s_branch .Lmjoin_c
.Lmd1_c:
	v_sub_u32_e32 v84, v219, v228
	v_mov_b32_e32 v67, v99
	v_mov_b32_e32 v66, v98
	v_mov_b32_e32 v68, v100
	v_mov_b32_e32 v69, v101
	v_mov_b32_e32 v70, v102
	v_mov_b32_e32 v71, v103
	v_mov_b32_e32 v72, v104
	v_mov_b32_e32 v73, v105
	v_mov_b32_e32 v74, v106
	v_mov_b32_e32 v75, v107
	v_mov_b32_e32 v76, v108
	v_mov_b32_e32 v77, v109
	v_mov_b32_e32 v78, v110
	v_mov_b32_e32 v79, v111
	v_mov_b32_e32 v80, v112
	v_mov_b32_e32 v81, v113
	v_cmp_le_i32_e32 vcc, 0xe0, v84
	s_nop 1
	v_cndmask_b32_e32 v50, v241, v50, vcc
	v_cmp_le_i32_e32 vcc, 0xe1, v84
	s_nop 1
	v_cndmask_b32_e32 v51, v241, v51, vcc
	v_cmp_le_i32_e32 vcc, 0xe2, v84
	s_nop 1
	v_cndmask_b32_e32 v52, v241, v52, vcc
	v_cmp_le_i32_e32 vcc, 0xe3, v84
	s_nop 1
	v_cndmask_b32_e32 v53, v241, v53, vcc
	v_cmp_le_i32_e32 vcc, 0xe8, v84
	s_nop 1
	v_cndmask_b32_e32 v54, v241, v54, vcc
	v_cmp_le_i32_e32 vcc, 0xe9, v84
	s_nop 1
	v_cndmask_b32_e32 v55, v241, v55, vcc
	v_cmp_le_i32_e32 vcc, 0xea, v84
	s_nop 1
	v_cndmask_b32_e32 v56, v241, v56, vcc
	v_cmp_le_i32_e32 vcc, 0xeb, v84
	s_nop 1
	v_cndmask_b32_e32 v57, v241, v57, vcc
	v_cmp_le_i32_e32 vcc, 0xf0, v84
	s_nop 1
	v_cndmask_b32_e32 v58, v241, v58, vcc
	v_cmp_le_i32_e32 vcc, 0xf1, v84
	s_nop 1
	v_cndmask_b32_e32 v59, v241, v59, vcc
	v_cmp_le_i32_e32 vcc, 0xf2, v84
	s_nop 1
	v_cndmask_b32_e32 v60, v241, v60, vcc
	v_cmp_le_i32_e32 vcc, 0xf3, v84
	s_nop 1
	v_cndmask_b32_e32 v61, v241, v61, vcc
	v_cmp_le_i32_e32 vcc, 0xf8, v84
	s_nop 1
	v_cndmask_b32_e32 v62, v241, v62, vcc
	v_cmp_le_i32_e32 vcc, 0xf9, v84
	s_nop 1
	v_cndmask_b32_e32 v63, v241, v63, vcc
	v_cmp_le_i32_e32 vcc, 0xfa, v84
	s_nop 1
	v_cndmask_b32_e32 v64, v241, v64, vcc
	v_cmp_le_i32_e32 vcc, 0xfb, v84
	s_nop 1
	v_cndmask_b32_e32 v65, v241, v65, vcc
.Lmjoin_c:
	v_max_f32_e32 v84, v66, v66
	v_add_f32_e32 v98, v242, v82
	v_max_f32_e32 v83, v67, v67
	v_max_f32_e32 v83, v84, v83
	v_max3_f32 v84, v68, v69, v51
	v_max3_f32 v83, v83, v50, v52
	v_max3_f32 v83, v83, v53, v70
	v_max3_f32 v84, v84, v72, v73
	v_max3_f32 v83, v83, v71, v54
	v_max3_f32 v84, v84, v56, v57
	v_max3_f32 v83, v83, v55, v74
	v_max3_f32 v84, v84, v76, v77
	v_max3_f32 v83, v83, v75, v58
	v_max3_f32 v84, v84, v60, v61
	v_max3_f32 v83, v83, v59, v78
	v_max3_f32 v84, v84, v80, v81
	v_max3_f32 v83, v83, v79, v62
	v_max3_f32 v84, v84, v64, v65
	v_max3_f32 v82, v83, v63, v84
	v_mov_b32_e32 v83, v82
	s_nop 1
	v_permlane32_swap_b32_e32 v82, v83
	v_max_f32_e32 v82, v82, v83
	v_cmp_lt_f32_e32 vcc, s34, v82
	s_cmp_lg_u64 vcc, 0
	s_cselect_b64 s[2:3], -1, 0
	s_cbranch_vccnz .LBB3_77
